# baseline (speedup 1.0000x reference)
.LBB1_8:
	s_or_b64 exec, exec, s[4:5]
	v_add_u32_e32 v10, v172, v2
	s_waitcnt vmcnt(1) lgkmcnt(0)
	s_barrier
	v_readfirstlane_b32 s4, v0
	s_cmp_lt_u32 s4, 256
	s_cbranch_scc1 .Lno_stagger
	s_sleep 4
.Lno_stagger:
	ds_read_b128 v[18:21], v10 offset:256
	ds_read_b128 v[22:25], v10 offset:288
	ds_read_b128 v[82:85], v10 offset:320
	ds_read_b128 v[86:89], v10 offset:352
	ds_read_b128 v[74:77], v10 offset:384
	ds_read_b128 v[78:81], v10 offset:416
	ds_read_b128 v[2:5], v213 offset:32768
	ds_read_b128 v[6:9], v213 offset:0
	ds_read_b128 v[66:69], v10 offset:448
	ds_read_b128 v[70:73], v10 offset:480
	ds_read_b128 v[10:13], v213 offset:1024
	s_waitcnt lgkmcnt(3)
	v_pk_mul_f32 v[26:27], v[8:9], v[20:21]
	v_pk_mul_f32 v[28:29], v[6:7], v[18:19]
	ds_read_b128 v[14:17], v213 offset:8192
	s_waitcnt lgkmcnt(1)
	v_pk_mul_f32 v[12:13], v[12:13], v[24:25]
	v_pk_mul_f32 v[10:11], v[10:11], v[22:23]
	v_pk_fma_f32 v[30:31], v[8:9], v[20:21], v[12:13]
	v_pk_fma_f32 v[32:33], v[6:7], v[18:19], v[10:11]
	v_cvt_pk_bf16_f32 v9, v12, v13
	v_cvt_pk_bf16_f32 v7, v26, v27
	v_cvt_pk_bf16_f32 v8, v10, v11
	v_cvt_pk_bf16_f32 v6, v28, v29
	ds_read_b128 v[10:13], v213 offset:33792
	s_nop 0
	v_mfma_f32_32x32x16_bf16 v[34:49], v[2:5], v[6:9], 0
	ds_read_b128 v[6:9], v213 offset:9216
	s_waitcnt lgkmcnt(2)
	v_mul_f32_e32 v26, v16, v20
	v_mul_f32_e32 v27, v17, v21
	v_pk_mul_f32 v[50:51], v[14:15], v[18:19]
	s_mov_b32 s4, 0x3727c5ac
	s_waitcnt lgkmcnt(0)
	v_pk_mul_f32 v[8:9], v[8:9], v[24:25]
	v_pk_mul_f32 v[28:29], v[6:7], v[22:23]
	v_pk_fma_f32 v[90:91], v[16:17], v[20:21], v[8:9]
	v_pk_fma_f32 v[92:93], v[14:15], v[18:19], v[28:29]
	ds_read_b128 v[14:17], v213 offset:2048
	v_cvt_pk_bf16_f32 v9, v8, v9
	v_cvt_pk_bf16_f32 v7, v26, v27
	v_cvt_pk_bf16_f32 v8, v28, v29
	ds_read_b128 v[26:29], v213 offset:3072
	v_cvt_pk_bf16_f32 v6, v50, v51
	s_waitcnt lgkmcnt(1)
	v_pk_mul_f32 v[94:95], v[14:15], v[82:83]
	s_mov_b32 s0, 0x3c800000
	v_mfma_f32_32x32x16_bf16 v[50:65], v[2:5], v[6:9], 0
	v_mul_f32_e32 v2, v16, v84
	v_mul_f32_e32 v3, v17, v85
	s_waitcnt lgkmcnt(0)
	v_mul_f32_e32 v4, v28, v88
	v_mul_f32_e32 v5, v29, v89
	v_pk_mul_f32 v[6:7], v[26:27], v[86:87]
	v_pk_fma_f32 v[8:9], v[16:17], v[84:85], v[4:5]
	v_cvt_pk_bf16_f32 v3, v2, v3
	v_pk_fma_f32 v[14:15], v[14:15], v[82:83], v[6:7]
	v_pk_add_f32 v[26:27], v[8:9], v[30:31]
	v_cvt_pk_bf16_f32 v5, v4, v5
	v_cvt_pk_bf16_f32 v4, v6, v7
	ds_read_b128 v[6:9], v213 offset:10240
	v_pk_add_f32 v[28:29], v[14:15], v[32:33]
	ds_read_b128 v[14:17], v213 offset:11264
	v_cvt_pk_bf16_f32 v2, v94, v95
	s_waitcnt lgkmcnt(1)
	v_pk_mul_f32 v[30:31], v[6:7], v[82:83]
	v_mov_b64_e32 v[152:153], s[4:5]
	v_mfma_f32_32x32x16_bf16 v[34:49], v[10:13], v[2:5], v[34:49]
	v_mul_f32_e32 v2, v8, v84
	v_mul_f32_e32 v3, v9, v85
	s_waitcnt lgkmcnt(0)
	v_mul_f32_e32 v4, v16, v88
	v_mul_f32_e32 v5, v17, v89
	v_pk_mul_f32 v[14:15], v[14:15], v[86:87]
	v_pk_fma_f32 v[8:9], v[8:9], v[84:85], v[4:5]
	v_pk_fma_f32 v[6:7], v[6:7], v[82:83], v[14:15]
	v_cvt_pk_bf16_f32 v5, v4, v5
	v_cvt_pk_bf16_f32 v3, v2, v3
	v_cvt_pk_bf16_f32 v4, v14, v15
	v_pk_add_f32 v[32:33], v[8:9], v[90:91]
	v_pk_add_f32 v[90:91], v[6:7], v[92:93]
	ds_read_b128 v[6:9], v213 offset:34816
	ds_read_b128 v[14:17], v213 offset:4096
	v_cvt_pk_bf16_f32 v2, v30, v31
	s_mov_b32 s13, 0
	s_mov_b64 s[6:7], 0
	v_mfma_f32_32x32x16_bf16 v[50:65], v[10:13], v[2:5], v[50:65]
	ds_read_b128 v[2:5], v213 offset:5120
	ds_read_b128 v[10:13], v213 offset:12288
	s_waitcnt lgkmcnt(2)
	v_pk_mul_f32 v[30:31], v[16:17], v[76:77]
	v_pk_mul_f32 v[92:93], v[14:15], v[74:75]
	s_waitcnt lgkmcnt(1)
	v_pk_mul_f32 v[4:5], v[4:5], v[80:81]
	v_pk_mul_f32 v[94:95], v[2:3], v[78:79]
	v_pk_fma_f32 v[2:3], v[16:17], v[76:77], v[4:5]
	v_cvt_pk_bf16_f32 v5, v4, v5
	v_pk_add_f32 v[96:97], v[2:3], v[26:27]
	v_cvt_pk_bf16_f32 v3, v30, v31
	v_cvt_pk_bf16_f32 v4, v94, v95
	v_cvt_pk_bf16_f32 v2, v92, v93
	v_pk_fma_f32 v[14:15], v[14:15], v[74:75], v[94:95]
	s_waitcnt lgkmcnt(0)
	v_pk_mul_f32 v[30:31], v[10:11], v[74:75]
	v_mfma_f32_32x32x16_bf16 v[34:49], v[6:9], v[2:5], v[34:49]
	ds_read_b128 v[2:5], v213 offset:13312
	v_add_f32_e32 v98, v14, v28
	v_add_f32_e32 v99, v15, v29
	ds_read_b128 v[14:17], v213 offset:35840
	v_pk_mul_f32 v[26:27], v[12:13], v[76:77]
	s_waitcnt lgkmcnt(1)
	v_pk_mul_f32 v[4:5], v[4:5], v[80:81]
	v_pk_mul_f32 v[28:29], v[2:3], v[78:79]
	v_pk_fma_f32 v[2:3], v[12:13], v[76:77], v[4:5]
	v_pk_fma_f32 v[10:11], v[10:11], v[74:75], v[28:29]
	v_pk_add_f32 v[32:33], v[2:3], v[32:33]
	v_pk_add_f32 v[92:93], v[10:11], v[90:91]
	ds_read_b128 v[10:13], v213 offset:6144
	v_cvt_pk_bf16_f32 v5, v4, v5
	v_cvt_pk_bf16_f32 v3, v26, v27
	v_cvt_pk_bf16_f32 v4, v28, v29
	ds_read_b128 v[26:29], v213 offset:7168
	v_cvt_pk_bf16_f32 v2, v30, v31
	s_waitcnt lgkmcnt(1)
	v_pk_mul_f32 v[30:31], v[10:11], v[66:67]
	v_mfma_f32_32x32x16_bf16 v[50:65], v[6:9], v[2:5], v[50:65]
	v_mul_f32_e32 v2, v12, v68
	v_mul_f32_e32 v3, v13, v69
	s_waitcnt lgkmcnt(0)
	v_mul_f32_e32 v4, v28, v72
	v_mul_f32_e32 v5, v29, v73
	v_pk_mul_f32 v[6:7], v[26:27], v[70:71]
	v_pk_fma_f32 v[8:9], v[12:13], v[68:69], v[4:5]
	v_cvt_pk_bf16_f32 v3, v2, v3
	v_pk_fma_f32 v[10:11], v[10:11], v[66:67], v[6:7]
	v_pk_add_f32 v[94:95], v[8:9], v[96:97]
	v_cvt_pk_bf16_f32 v5, v4, v5
	v_cvt_pk_bf16_f32 v4, v6, v7
	ds_read_b128 v[6:9], v213 offset:14336
	v_pk_add_f32 v[96:97], v[10:11], v[98:99]
	ds_read_b128 v[10:13], v213 offset:15360
	v_cvt_pk_bf16_f32 v2, v30, v31
	s_waitcnt lgkmcnt(1)
	v_pk_mul_f32 v[30:31], v[6:7], v[66:67]
	v_mfma_f32_32x32x16_bf16 v[34:49], v[14:17], v[2:5], v[34:49]
	s_waitcnt lgkmcnt(0)
	v_mul_f32_e32 v10, v10, v70
	v_mul_f32_e32 v11, v11, v71
	v_mul_f32_e32 v2, v8, v68
	v_mul_f32_e32 v3, v9, v69
	v_pk_mul_f32 v[4:5], v[12:13], v[72:73]
	v_pk_fma_f32 v[6:7], v[6:7], v[66:67], v[10:11]
	v_pk_fma_f32 v[8:9], v[8:9], v[68:69], v[4:5]
	v_pk_add_f32 v[92:93], v[6:7], v[92:93]
	v_cvt_pk_bf16_f32 v3, v2, v3
	v_pk_add_f32 v[90:91], v[8:9], v[32:33]
	v_cvt_pk_bf16_f32 v5, v4, v5
	v_cvt_pk_bf16_f32 v4, v10, v11
	ds_read_b128 v[26:29], v213 offset:36864
	ds_read_b128 v[6:9], v213 offset:16384
	v_cvt_pk_bf16_f32 v2, v30, v31
	ds_read_b128 v[98:101], v213 offset:25600
	ds_read_b128 v[102:105], v213 offset:37888
	v_mfma_f32_32x32x16_bf16 v[50:65], v[14:17], v[2:5], v[50:65]
	ds_read_b128 v[2:5], v213 offset:17408
	ds_read_b128 v[30:33], v213 offset:24576
	s_waitcnt lgkmcnt(4)
	v_pk_mul_f32 v[12:13], v[6:7], v[18:19]
	v_pk_mul_f32 v[10:11], v[8:9], v[20:21]
	s_waitcnt lgkmcnt(1)
	v_pk_mul_f32 v[14:15], v[2:3], v[22:23]
	v_pk_mul_f32 v[22:23], v[98:99], v[22:23]
	v_pk_fma_f32 v[112:113], v[6:7], v[18:19], v[14:15]
	s_waitcnt lgkmcnt(0)
	v_pk_mul_f32 v[114:115], v[30:31], v[18:19]
	v_pk_fma_f32 v[118:119], v[30:31], v[18:19], v[22:23]
	v_pk_mul_f32 v[4:5], v[4:5], v[24:25]
	v_pk_mul_f32 v[106:107], v[32:33], v[20:21]
	v_pk_mul_f32 v[24:25], v[100:101], v[24:25]
	ds_read_b128 v[98:101], v213 offset:18432
	v_cvt_pk_bf16_f32 v19, v106, v107
	ds_read_b128 v[106:109], v213 offset:19456
	v_pk_fma_f32 v[110:111], v[8:9], v[20:21], v[4:5]
	v_cvt_pk_bf16_f32 v5, v4, v5
	v_cvt_pk_bf16_f32 v3, v10, v11
	v_cvt_pk_bf16_f32 v4, v14, v15
	s_waitcnt lgkmcnt(0)
	v_pk_mul_f32 v[106:107], v[106:107], v[86:87]
	v_cvt_pk_bf16_f32 v2, v12, v13
	v_pk_mul_f32 v[120:121], v[98:99], v[82:83]
	v_pk_mul_f32 v[108:109], v[108:109], v[88:89]
	v_pk_fma_f32 v[98:99], v[98:99], v[82:83], v[106:107]
	v_mfma_f32_32x32x16_bf16 v[2:17], v[26:29], v[2:5], 0
	v_cvt_pk_bf16_f32 v18, v114, v115
	v_mul_f32_e32 v114, v100, v84
	v_mul_f32_e32 v115, v101, v85
	v_fma_f32 v100, v100, v84, v108
	v_fma_f32 v101, v101, v85, v109
	v_pk_add_f32 v[124:125], v[98:99], v[112:113]
	v_pk_add_f32 v[122:123], v[100:101], v[110:111]
	v_cvt_pk_bf16_f32 v101, v108, v109
	v_cvt_pk_bf16_f32 v100, v106, v107
	ds_read_b128 v[106:109], v213 offset:26624
	v_pk_fma_f32 v[116:117], v[32:33], v[20:21], v[24:25]
	v_cvt_pk_bf16_f32 v21, v24, v25
	v_cvt_pk_bf16_f32 v20, v22, v23
	ds_read_b128 v[110:113], v213 offset:27648
	v_cvt_pk_bf16_f32 v99, v114, v115
	v_mfma_f32_32x32x16_bf16 v[18:33], v[26:29], v[18:21], 0
	v_cvt_pk_bf16_f32 v98, v120, v121
	s_waitcnt lgkmcnt(1)
	v_mul_f32_e32 v114, v106, v82
	v_mul_f32_e32 v115, v107, v83
	s_waitcnt lgkmcnt(0)
	v_pk_mul_f32 v[86:87], v[110:111], v[86:87]
	v_pk_mul_f32 v[88:89], v[112:113], v[88:89]
	v_pk_fma_f32 v[82:83], v[106:107], v[82:83], v[86:87]
	v_mfma_f32_32x32x16_bf16 v[2:17], v[102:105], v[98:101], v[2:17]
	v_mul_f32_e32 v98, v108, v84
	v_mul_f32_e32 v99, v109, v85
	v_fma_f32 v84, v108, v84, v88
	v_fma_f32 v85, v109, v85, v89
	v_add_f32_e32 v108, v82, v118
	v_add_f32_e32 v109, v83, v119
	v_cvt_pk_bf16_f32 v83, v98, v99
	v_pk_add_f32 v[106:107], v[84:85], v[116:117]
	v_cvt_pk_bf16_f32 v85, v88, v89
	v_cvt_pk_bf16_f32 v84, v86, v87
	ds_read_b128 v[86:89], v213 offset:38912
	ds_read_b128 v[98:101], v213 offset:20480
	v_cvt_pk_bf16_f32 v82, v114, v115
	s_waitcnt lgkmcnt(0)
	v_pk_mul_f32 v[110:111], v[100:101], v[76:77]
	v_mfma_f32_32x32x16_bf16 v[18:33], v[102:105], v[82:85], v[18:33]
	ds_read_b128 v[82:85], v213 offset:21504
	ds_read_b128 v[102:105], v213 offset:28672
	v_mul_f32_e32 v112, v98, v74
	v_mul_f32_e32 v113, v99, v75
	s_waitcnt lgkmcnt(1)
	v_pk_mul_f32 v[84:85], v[84:85], v[80:81]
	v_pk_mul_f32 v[114:115], v[82:83], v[78:79]
	v_pk_fma_f32 v[82:83], v[100:101], v[76:77], v[84:85]
	v_cvt_pk_bf16_f32 v85, v84, v85
	v_pk_add_f32 v[116:117], v[82:83], v[122:123]
	v_cvt_pk_bf16_f32 v83, v110, v111
	v_cvt_pk_bf16_f32 v84, v114, v115
	v_cvt_pk_bf16_f32 v82, v112, v113
	v_pk_fma_f32 v[98:99], v[98:99], v[74:75], v[114:115]
	s_waitcnt lgkmcnt(0)
	v_pk_mul_f32 v[112:113], v[102:103], v[74:75]
	v_mfma_f32_32x32x16_bf16 v[2:17], v[86:89], v[82:85], v[2:17]
	ds_read_b128 v[82:85], v213 offset:29696
	v_add_f32_e32 v118, v98, v124
	v_add_f32_e32 v119, v99, v125
	v_mul_f32_e32 v110, v104, v76
	v_mul_f32_e32 v111, v105, v77
	ds_read_b128 v[98:101], v213 offset:39936
	s_waitcnt lgkmcnt(1)
	v_pk_mul_f32 v[78:79], v[82:83], v[78:79]
	v_pk_mul_f32 v[80:81], v[84:85], v[80:81]
	v_pk_fma_f32 v[74:75], v[102:103], v[74:75], v[78:79]
	v_pk_fma_f32 v[76:77], v[104:105], v[76:77], v[80:81]
	v_pk_add_f32 v[104:105], v[74:75], v[108:109]
	v_pk_add_f32 v[102:103], v[76:77], v[106:107]
	v_cvt_pk_bf16_f32 v77, v80, v81
	v_cvt_pk_bf16_f32 v76, v78, v79
	ds_read_b128 v[78:81], v213 offset:22528
	ds_read_b128 v[82:85], v213 offset:23552
	v_cvt_pk_bf16_f32 v75, v110, v111
	v_cvt_pk_bf16_f32 v74, v112, v113
	s_waitcnt lgkmcnt(0)
	v_pk_mul_f32 v[82:83], v[82:83], v[70:71]
	v_mfma_f32_32x32x16_bf16 v[18:33], v[86:89], v[74:77], v[18:33]
	v_mul_f32_e32 v74, v80, v68
	v_mul_f32_e32 v75, v81, v69
	v_mul_f32_e32 v76, v84, v72
	v_mul_f32_e32 v77, v85, v73
	v_mul_f32_e32 v86, v78, v66
	v_mul_f32_e32 v87, v79, v67
	v_pk_fma_f32 v[80:81], v[80:81], v[68:69], v[76:77]
	v_pk_fma_f32 v[78:79], v[78:79], v[66:67], v[82:83]
	v_cvt_pk_bf16_f32 v75, v74, v75
	v_pk_add_f32 v[88:89], v[80:81], v[116:117]
	v_pk_add_f32 v[106:107], v[78:79], v[118:119]
	ds_read_b128 v[78:81], v213 offset:30720
	v_cvt_pk_bf16_f32 v77, v76, v77
	v_cvt_pk_bf16_f32 v76, v82, v83
	ds_read_b128 v[82:85], v213 offset:31744
	v_cvt_pk_bf16_f32 v74, v86, v87
	s_waitcnt lgkmcnt(0)
	v_pk_mul_f32 v[72:73], v[84:85], v[72:73]
	v_mfma_f32_32x32x16_bf16 v[2:17], v[98:101], v[74:77], v[2:17]
	v_mul_f32_e32 v74, v80, v68
	v_mul_f32_e32 v75, v81, v69
	v_fma_f32 v68, v80, v68, v72
	v_fma_f32 v69, v81, v69, v73
	v_mul_f32_e32 v70, v82, v70
	v_mul_f32_e32 v71, v83, v71
	v_pk_add_f32 v[84:85], v[68:69], v[102:103]
	v_cvt_pk_bf16_f32 v69, v72, v73
	v_pk_mov_b32 v[72:73], v[96:97], v[94:95] op_sel:[1,0]
	v_mov_b32_e32 v97, v95
	v_pk_add_f32 v[72:73], v[72:73], v[96:97]
	v_pk_mul_f32 v[76:77], v[78:79], v[66:67]
	v_pk_fma_f32 v[66:67], v[78:79], v[66:67], v[70:71]
	v_pk_add_f32 v[72:73], v[72:73], v[72:73] op_sel:[0,1] op_sel_hi:[1,0]
	v_pk_add_f32 v[86:87], v[66:67], v[104:105]
	v_mov_b32_e32 v66, v72
	s_nop 1
	v_permlane32_swap_b32_e32 v72, v66
	v_add_f32_e32 v66, v72, v66
	v_cvt_pk_bf16_f32 v67, v74, v75
	v_rcp_f32_e32 v74, v66
	v_cvt_pk_bf16_f32 v68, v70, v71
	v_cvt_pk_bf16_f32 v66, v76, v77
	v_pk_mul_f32 v[70:71], v[46:47], v[74:75] op_sel_hi:[1,0]
	s_nop 0
	v_mfma_f32_32x32x16_bf16 v[18:33], v[98:101], v[66:69], v[18:33]
	v_mul_f32_e32 v66, v42, v74
	v_mul_f32_e32 v67, v43, v74
	v_pk_mov_b32 v[42:43], v[92:93], v[90:91] op_sel:[1,0]
	v_mov_b32_e32 v93, v91
	v_pk_add_f32 v[42:43], v[42:43], v[92:93]
	v_pk_mul_f32 v[68:69], v[44:45], v[74:75] op_sel_hi:[1,0]
	v_pk_add_f32 v[42:43], v[42:43], v[42:43] op_sel:[0,1] op_sel_hi:[1,0]
	v_pk_mov_b32 v[44:45], v[106:107], v[88:89] op_sel:[1,0]
	v_mov_b32_e32 v43, v42
	s_nop 1
	v_permlane32_swap_b32_e32 v42, v43
	v_add_f32_e32 v42, v42, v43
	v_rcp_f32_e32 v42, v42
	v_mov_b32_e32 v107, v89
	v_pk_add_f32 v[44:45], v[44:45], v[106:107]
	v_pk_mul_f32 v[72:73], v[48:49], v[74:75] op_sel_hi:[1,0]
	v_pk_add_f32 v[44:45], v[44:45], v[44:45] op_sel:[0,1] op_sel_hi:[1,0]
	v_pk_mul_f32 v[36:37], v[36:37], v[74:75] op_sel_hi:[1,0]
	v_pk_mul_f32 v[38:39], v[38:39], v[74:75] op_sel_hi:[1,0]
	v_pk_mul_f32 v[40:41], v[40:41], v[74:75] op_sel_hi:[1,0]
	v_pk_mul_f32 v[34:35], v[34:35], v[74:75] op_sel_hi:[1,0]
	v_pk_mul_f32 v[74:75], v[58:59], v[42:43] op_sel_hi:[1,0]
	v_pk_mul_f32 v[78:79], v[60:61], v[42:43] op_sel_hi:[1,0]
	v_pk_mul_f32 v[80:81], v[62:63], v[42:43] op_sel_hi:[1,0]
	v_pk_mul_f32 v[82:83], v[64:65], v[42:43] op_sel_hi:[1,0]
	v_pk_mul_f32 v[92:93], v[52:53], v[42:43] op_sel_hi:[1,0]
	v_mov_b32_e32 v43, v44
	s_nop 1
	v_permlane32_swap_b32_e32 v44, v43
	v_add_f32_e32 v43, v44, v43
	v_rcp_f32_e32 v76, v43
	v_pk_mul_f32 v[96:97], v[54:55], v[42:43] op_sel_hi:[1,0]
	v_pk_mul_f32 v[94:95], v[56:57], v[42:43] op_sel_hi:[1,0]
	v_pk_mul_f32 v[98:99], v[50:51], v[42:43] op_sel_hi:[1,0]
	v_pk_mul_f32 v[100:101], v[4:5], v[76:77] op_sel_hi:[1,0]
	v_pk_mov_b32 v[4:5], v[86:87], v[84:85] op_sel:[1,0]
	v_mov_b32_e32 v87, v85
	v_pk_add_f32 v[4:5], v[4:5], v[86:87]
	v_pk_mul_f32 v[102:103], v[6:7], v[76:77] op_sel_hi:[1,0]
	v_pk_add_f32 v[104:105], v[4:5], v[4:5] op_sel:[0,1] op_sel_hi:[1,0]
	v_cvt_pk_bf16_f32 v7, v40, v41
	ds_read_b128 v[84:87], v150 offset:52224
	ds_read_b128 v[50:53], v150 offset:35840
	ds_read_b128 v[54:57], v150 offset:36864
	ds_read_b128 v[58:61], v150 offset:37888
	ds_read_b128 v[62:65], v150 offset:38912
	v_cvt_pk_bf16_f32 v6, v38, v39
	v_cvt_pk_bf16_f32 v5, v36, v37
	v_cvt_pk_bf16_f32 v4, v34, v35
	ds_read_b128 v[88:91], v150 offset:53248
	ds_read_b128 v[34:37], v150 offset:39936
	ds_read_b128 v[38:41], v150 offset:40960
	ds_read_b128 v[42:45], v150 offset:41984
	ds_read_b128 v[46:49], v150 offset:43008
	v_cvt_pk_bf16_f32 v95, v94, v95
	v_cvt_pk_bf16_f32 v94, v96, v97
	v_cvt_pk_bf16_f32 v93, v92, v93
	v_cvt_pk_bf16_f32 v92, v98, v99
	s_waitcnt lgkmcnt(5)
	v_mfma_f32_32x32x16_bf16 v[50:65], v[84:87], v[4:7], v[50:65]
	v_mul_f32_e32 v10, v10, v76
	v_mul_f32_e32 v11, v11, v76
	v_mul_f32_e32 v12, v12, v76
	v_mul_f32_e32 v13, v13, v76
	v_mul_f32_e32 v8, v8, v76
	v_mul_f32_e32 v9, v9, v76
	v_mov_b32_e32 v77, v104
	s_nop 1
	v_permlane32_swap_b32_e32 v104, v77
	v_cvt_pk_bf16_f32 v73, v72, v73
	s_waitcnt lgkmcnt(0)
	v_mfma_f32_32x32x16_bf16 v[34:49], v[84:87], v[92:95], v[34:49]
	v_cvt_pk_bf16_f32 v72, v70, v71
	v_cvt_pk_bf16_f32 v70, v66, v67
	v_add_f32_e32 v66, v104, v77
	v_cvt_pk_bf16_f32 v71, v68, v69
	v_rcp_f32_e32 v104, v66
	v_cvt_pk_bf16_f32 v69, v82, v83
	v_cvt_pk_bf16_f32 v68, v80, v81
	v_cvt_pk_bf16_f32 v67, v78, v79
	v_cvt_pk_bf16_f32 v66, v74, v75
	ds_read_b128 v[78:81], v150 offset:54272
	v_mfma_f32_32x32x16_bf16 v[50:65], v[88:91], v[70:73], v[50:65]
	v_mul_f32_e32 v2, v2, v76
	v_mul_f32_e32 v3, v3, v76
	v_mul_f32_e32 v20, v20, v104
	v_mul_f32_e32 v21, v21, v104
	v_cvt_pk_bf16_f32 v85, v8, v9
	v_cvt_pk_bf16_f32 v82, v2, v3
	v_pk_mul_f32 v[2:3], v[22:23], v[104:105] op_sel_hi:[1,0]
	v_pk_mul_f32 v[8:9], v[24:25], v[104:105] op_sel_hi:[1,0]
	v_pk_mul_f32 v[18:19], v[18:19], v[104:105] op_sel_hi:[1,0]
	v_mfma_f32_32x32x16_bf16 v[34:49], v[88:91], v[66:69], v[34:49]
	v_cvt_pk_bf16_f32 v84, v102, v103
	v_cvt_pk_bf16_f32 v83, v100, v101
	ds_read_b128 v[86:89], v150 offset:55296
	v_cvt_pk_bf16_f32 v99, v8, v9
	v_cvt_pk_bf16_f32 v98, v2, v3
	v_cvt_pk_bf16_f32 v97, v20, v21
	v_cvt_pk_bf16_f32 v96, v18, v19
	s_waitcnt lgkmcnt(1)
	v_mfma_f32_32x32x16_bf16 v[50:65], v[78:81], v[82:85], v[50:65]
	v_mul_f32_e32 v2, v14, v76
	v_mul_f32_e32 v3, v15, v76
	v_mul_f32_e32 v8, v16, v76
	v_mul_f32_e32 v9, v17, v76
	v_mul_f32_e32 v14, v26, v104
	v_mul_f32_e32 v15, v27, v104
	v_cvt_pk_bf16_f32 v77, v8, v9
	v_cvt_pk_bf16_f32 v76, v2, v3
	v_cvt_pk_bf16_f32 v74, v10, v11
	v_pk_mul_f32 v[2:3], v[28:29], v[104:105] op_sel_hi:[1,0]
	v_mfma_f32_32x32x16_bf16 v[34:49], v[78:81], v[96:99], v[34:49]
	v_mul_f32_e32 v8, v30, v104
	v_mul_f32_e32 v9, v31, v104
	v_mul_f32_e32 v10, v32, v104
	v_mul_f32_e32 v11, v33, v104
	v_cvt_pk_bf16_f32 v75, v12, v13
	v_cvt_pk_bf16_f32 v81, v10, v11
	v_cvt_pk_bf16_f32 v80, v8, v9
	v_cvt_pk_bf16_f32 v79, v2, v3
	v_cvt_pk_bf16_f32 v78, v14, v15
	s_waitcnt lgkmcnt(0)
	v_mfma_f32_32x32x16_bf16 v[50:65], v[86:89], v[74:77], v[50:65]
	v_mfma_f32_32x32x16_bf16 v[34:49], v[86:89], v[78:81], v[34:49]
	ds_read_b128 v[86:89], v150 offset:56320
	ds_read_b128 v[18:21], v150 offset:44032
	ds_read_b128 v[22:25], v150 offset:45056
	ds_read_b128 v[26:29], v150 offset:46080
	ds_read_b128 v[30:33], v150 offset:47104
	ds_read_b128 v[100:103], v150 offset:57344
	s_waitcnt lgkmcnt(1)
	v_mfma_f32_32x32x16_bf16 v[18:33], v[86:89], v[4:7], v[18:33]
	ds_read_b128 v[2:5], v150 offset:48128
	ds_read_b128 v[6:9], v150 offset:49152
	ds_read_b128 v[10:13], v150 offset:50176
	ds_read_b128 v[14:17], v150 offset:51200
	s_waitcnt lgkmcnt(0)
	v_mfma_f32_32x32x16_bf16 v[2:17], v[86:89], v[92:95], v[2:17]
	v_mfma_f32_32x32x16_bf16 v[18:33], v[100:103], v[70:73], v[18:33]
	v_mfma_f32_32x32x16_bf16 v[2:17], v[100:103], v[66:69], v[2:17]
	ds_read_b128 v[66:69], v150 offset:58368
	ds_read_b128 v[70:73], v150 offset:59392
	s_waitcnt lgkmcnt(1)
	v_mfma_f32_32x32x16_bf16 v[18:33], v[66:69], v[82:85], v[18:33]
	v_mfma_f32_32x32x16_bf16 v[2:17], v[66:69], v[96:99], v[2:17]
	s_waitcnt lgkmcnt(0)
	v_mfma_f32_32x32x16_bf16 v[18:33], v[70:73], v[74:77], v[18:33]
	v_mfma_f32_32x32x16_bf16 v[2:17], v[70:73], v[78:81], v[2:17]
	s_nop 10
	v_mul_f32_e32 v66, v22, v22
	v_mul_f32_e32 v67, v23, v23
	v_mul_f32_e32 v68, v30, v30
	v_mul_f32_e32 v69, v31, v31
	v_mul_f32_e32 v70, v24, v24
	v_mul_f32_e32 v71, v25, v25
	v_pk_mul_f32 v[72:73], v[32:33], v[32:33]
	v_pk_mul_f32 v[74:75], v[20:21], v[20:21]
	v_pk_mul_f32 v[76:77], v[28:29], v[28:29]
	v_pk_mul_f32 v[78:79], v[26:27], v[26:27]
	v_pk_mul_f32 v[80:81], v[18:19], v[18:19]
	v_pk_fma_f32 v[78:79], v[58:59], v[58:59], v[78:79]
	v_pk_fma_f32 v[76:77], v[60:61], v[60:61], v[76:77]
	v_pk_fma_f32 v[74:75], v[52:53], v[52:53], v[74:75]
	v_pk_fma_f32 v[72:73], v[64:65], v[64:65], v[72:73]
	v_pk_fma_f32 v[70:71], v[56:57], v[56:57], v[70:71]
	v_pk_fma_f32 v[68:69], v[62:63], v[62:63], v[68:69]
	v_pk_fma_f32 v[66:67], v[54:55], v[54:55], v[66:67]
	v_pk_fma_f32 v[80:81], v[50:51], v[50:51], v[80:81]
	v_pk_add_f32 v[66:67], v[66:67], v[68:69]
	v_pk_add_f32 v[68:69], v[70:71], v[72:73]
	v_pk_add_f32 v[70:71], v[74:75], v[76:77]
	v_pk_add_f32 v[72:73], v[80:81], v[78:79]
	v_pk_add_f32 v[68:69], v[70:71], v[68:69]
	v_pk_add_f32 v[66:67], v[72:73], v[66:67]
	v_pk_mul_f32 v[72:73], v[14:15], v[14:15]
	v_pk_mov_b32 v[70:71], v[66:67], v[68:69] op_sel:[1,0]
	v_mov_b32_e32 v67, v69
	v_pk_add_f32 v[66:67], v[70:71], v[66:67]
	v_pk_mul_f32 v[70:71], v[6:7], v[6:7]
	v_pk_mul_f32 v[74:75], v[8:9], v[8:9]
	v_pk_mul_f32 v[76:77], v[16:17], v[16:17]
	v_pk_mul_f32 v[78:79], v[4:5], v[4:5]
	v_pk_mul_f32 v[80:81], v[12:13], v[12:13]
	v_pk_mul_f32 v[82:83], v[10:11], v[10:11]
	v_pk_mul_f32 v[84:85], v[2:3], v[2:3]
	v_pk_fma_f32 v[82:83], v[42:43], v[42:43], v[82:83]
	v_pk_fma_f32 v[80:81], v[44:45], v[44:45], v[80:81]
	v_pk_fma_f32 v[78:79], v[36:37], v[36:37], v[78:79]
	v_pk_fma_f32 v[76:77], v[48:49], v[48:49], v[76:77]
	v_pk_fma_f32 v[74:75], v[40:41], v[40:41], v[74:75]
	v_pk_fma_f32 v[72:73], v[46:47], v[46:47], v[72:73]
	v_pk_fma_f32 v[70:71], v[38:39], v[38:39], v[70:71]
	v_pk_fma_f32 v[84:85], v[34:35], v[34:35], v[84:85]
	v_pk_add_f32 v[70:71], v[70:71], v[72:73]
	v_pk_add_f32 v[72:73], v[74:75], v[76:77]
	v_pk_add_f32 v[74:75], v[78:79], v[80:81]
	v_pk_add_f32 v[76:77], v[84:85], v[82:83]
	v_pk_add_f32 v[72:73], v[74:75], v[72:73]
	v_pk_add_f32 v[70:71], v[76:77], v[70:71]
	v_pk_add_f32 v[66:67], v[66:67], v[66:67] op_sel:[0,1] op_sel_hi:[1,0]
	v_pk_mov_b32 v[74:75], v[70:71], v[72:73] op_sel:[1,0]
	v_mov_b32_e32 v71, v73
	v_pk_add_f32 v[70:71], v[74:75], v[70:71]
	v_mov_b32_e32 v69, v66
	v_pk_add_f32 v[70:71], v[70:71], v[70:71] op_sel:[0,1] op_sel_hi:[1,0]
	s_nop 0
	v_permlane32_swap_b32_e32 v66, v69
	v_mov_b32_e32 v68, v70
	s_nop 1
	v_permlane32_swap_b32_e32 v70, v68
	v_mov_b32_e32 v71, v66
	v_pk_add_f32 v[66:67], v[70:71], v[68:69]
	v_pk_fma_f32 v[66:67], v[66:67], s[0:1], v[152:153] op_sel_hi:[1,0,0]
	s_mov_b32 s1, 0x800000
	v_mul_f32_e32 v68, 0x4b800000, v67
	v_cmp_gt_f32_e32 vcc, s1, v67
	s_nop 1
	v_cndmask_b32_e32 v67, v67, v68, vcc
	v_rsq_f32_e32 v67, v67
	s_nop 0
	v_mul_f32_e32 v68, 0x45800000, v67
	v_cndmask_b32_e32 v68, v67, v68, vcc
	v_pk_mul_f32 v[158:159], v[50:51], v[68:69] op_sel_hi:[1,0]
	v_pk_mul_f32 v[50:51], v[18:19], v[68:69] op_sel_hi:[1,0]
	v_mul_f32_e32 v18, 0x4b800000, v66
	v_cmp_gt_f32_e32 vcc, s1, v66
	v_pk_mul_f32 v[80:81], v[60:61], v[68:69] op_sel_hi:[1,0]
	v_pk_mul_f32 v[60:61], v[28:29], v[68:69] op_sel_hi:[1,0]
	v_cndmask_b32_e32 v18, v66, v18, vcc
	v_rsq_f32_e32 v18, v18
	v_pk_mul_f32 v[78:79], v[58:59], v[68:69] op_sel_hi:[1,0]
	v_pk_mul_f32 v[160:161], v[52:53], v[68:69] op_sel_hi:[1,0]
	v_pk_mul_f32 v[82:83], v[54:55], v[68:69] op_sel_hi:[1,0]
	v_mul_f32_e32 v19, 0x45800000, v18
	v_cndmask_b32_e32 v28, v18, v19, vcc
	v_pk_mul_f32 v[168:169], v[56:57], v[68:69] op_sel_hi:[1,0]
	v_pk_mul_f32 v[58:59], v[26:27], v[68:69] op_sel_hi:[1,0]
	v_pk_mul_f32 v[52:53], v[20:21], v[68:69] op_sel_hi:[1,0]
	v_pk_mul_f32 v[54:55], v[22:23], v[68:69] op_sel_hi:[1,0]
	v_pk_mul_f32 v[56:57], v[24:25], v[68:69] op_sel_hi:[1,0]
	v_pk_mul_f32 v[18:19], v[42:43], v[28:29] op_sel_hi:[1,0]
	v_pk_mul_f32 v[20:21], v[44:45], v[28:29] op_sel_hi:[1,0]
	v_pk_mul_f32 v[22:23], v[46:47], v[28:29] op_sel_hi:[1,0]
	v_pk_mul_f32 v[26:27], v[48:49], v[28:29] op_sel_hi:[1,0]
	v_pk_mul_f32 v[162:163], v[34:35], v[28:29] op_sel_hi:[1,0]
	v_pk_mul_f32 v[164:165], v[36:37], v[28:29] op_sel_hi:[1,0]
	v_pk_mul_f32 v[166:167], v[38:39], v[28:29] op_sel_hi:[1,0]
	v_pk_mul_f32 v[24:25], v[40:41], v[28:29] op_sel_hi:[1,0]
	v_pk_mul_f32 v[104:105], v[2:3], v[28:29] op_sel_hi:[1,0]
	v_pk_mul_f32 v[112:113], v[4:5], v[28:29] op_sel_hi:[1,0]
	ds_read_b128 v[2:5], v150 offset:60416
	ds_read_b128 v[34:37], v174 offset:32768
	ds_read_b128 v[38:41], v174 offset:32800
	ds_read_b128 v[42:45], v174 offset:32832
	ds_read_b128 v[46:49], v174 offset:32864
	v_cvt_pk_bf16_f32 v129, v168, v169
	v_cvt_pk_bf16_f32 v128, v82, v83
	v_cvt_pk_bf16_f32 v127, v160, v161
	v_cvt_pk_bf16_f32 v126, v158, v159
	v_cvt_pk_bf16_f32 v137, v24, v25
	v_cvt_pk_bf16_f32 v136, v166, v167
	v_cvt_pk_bf16_f32 v135, v164, v165
	s_waitcnt lgkmcnt(0)
	v_mfma_f32_32x32x16_bf16 v[86:101], v[2:5], v[126:129], v[34:49]
	v_cvt_pk_bf16_f32 v134, v162, v163
	v_mul_f32_e32 v84, v62, v68
	v_mul_f32_e32 v85, v63, v68
	v_mul_f32_e32 v170, v64, v68
	v_mul_f32_e32 v171, v65, v68
	v_pk_mul_f32 v[62:63], v[30:31], v[68:69] op_sel_hi:[1,0]
	v_pk_mul_f32 v[64:65], v[32:33], v[68:69] op_sel_hi:[1,0]
	v_pk_mul_f32 v[116:117], v[6:7], v[28:29] op_sel_hi:[1,0]
	v_pk_mul_f32 v[154:155], v[8:9], v[28:29] op_sel_hi:[1,0]
	v_mfma_f32_32x32x16_bf16 v[34:49], v[2:5], v[134:137], v[34:49]
	ds_read_b128 v[6:9], v150 offset:61440
	ds_read_b128 v[66:69], v174 offset:32896
	ds_read_b128 v[106:109], v150 offset:64512
	v_cvt_pk_bf16_f32 v125, v170, v171
	v_cvt_pk_bf16_f32 v124, v84, v85
	v_cvt_pk_bf16_f32 v123, v80, v81
	v_cvt_pk_bf16_f32 v122, v78, v79
	v_cvt_pk_bf16_f32 v149, v26, v27
	v_cvt_pk_bf16_f32 v148, v22, v23
	v_cvt_pk_bf16_f32 v147, v20, v21
	v_cvt_pk_bf16_f32 v146, v18, v19
	s_waitcnt lgkmcnt(2)
	v_mfma_f32_32x32x16_bf16 v[86:101], v[6:9], v[122:125], v[86:101]
	v_mul_f32_e32 v102, v10, v28
	v_mul_f32_e32 v103, v11, v28
	v_mul_f32_e32 v110, v12, v28
	v_mul_f32_e32 v111, v13, v28
	v_mul_f32_e32 v114, v14, v28
	v_mul_f32_e32 v115, v15, v28
	v_pk_mul_f32 v[156:157], v[16:17], v[28:29] op_sel_hi:[1,0]
	ds_read_b128 v[176:179], v174 offset:33536
	ds_read_b128 v[180:183], v174 offset:33568
	ds_read_b128 v[184:187], v174 offset:33600
	ds_read_b128 v[28:31], v174 offset:33632
	ds_read_b128 v[188:191], v174 offset:33792
	ds_read_b128 v[192:195], v174 offset:33824
	ds_read_b128 v[196:199], v174 offset:33856
	ds_read_b128 v[200:203], v174 offset:33888
	ds_read_b128 v[204:207], v150 offset:62464
	v_cvt_pk_bf16_f32 v133, v56, v57
	v_mfma_f32_32x32x16_bf16 v[34:49], v[6:9], v[146:149], v[34:49]
	v_cvt_pk_bf16_f32 v132, v54, v55
	v_cvt_pk_bf16_f32 v131, v52, v53
	v_cvt_pk_bf16_f32 v130, v50, v51
	ds_read_b128 v[70:73], v174 offset:33664
	ds_read_b128 v[74:77], v174 offset:33920
	ds_read_b128 v[208:211], v150 offset:63488
	v_cvt_pk_bf16_f32 v145, v154, v155
	v_cvt_pk_bf16_f32 v144, v116, v117
	v_cvt_pk_bf16_f32 v143, v112, v113
	v_cvt_pk_bf16_f32 v142, v104, v105
	s_waitcnt lgkmcnt(3)
	v_mfma_f32_32x32x16_bf16 v[86:101], v[204:207], v[130:133], v[86:101]
	v_cvt_pk_bf16_f32 v121, v64, v65
	v_cvt_pk_bf16_f32 v120, v62, v63
	v_cvt_pk_bf16_f32 v119, v60, v61
	v_cvt_pk_bf16_f32 v118, v58, v59
	v_cvt_pk_bf16_f32 v141, v156, v157
	v_cvt_pk_bf16_f32 v140, v114, v115
	v_cvt_pk_bf16_f32 v139, v110, v111
	v_mfma_f32_32x32x16_bf16 v[34:49], v[204:207], v[142:145], v[34:49]
	v_cvt_pk_bf16_f32 v138, v102, v103
	v_fma_f32 v16, v30, v170, v202
	v_fma_f32 v17, v31, v171, v203
	v_fma_f32 v14, v28, v84, v200
	v_fma_f32 v15, v29, v85, v201
	v_pk_fma_f32 v[12:13], v[186:187], v[80:81], v[198:199]
	v_pk_fma_f32 v[10:11], v[184:185], v[78:79], v[196:197]
	v_pk_fma_f32 v[8:9], v[182:183], v[168:169], v[194:195]
	s_waitcnt lgkmcnt(0)
	v_mfma_f32_32x32x16_bf16 v[86:101], v[208:211], v[118:121], v[86:101]
	v_fma_f32 v6, v180, v82, v192
	v_fma_f32 v7, v181, v83, v193
	ds_read_b128 v[78:81], v174 offset:33760
	ds_read_b128 v[82:85], v174 offset:33248
	v_fma_f32 v4, v178, v160, v190
	v_fma_f32 v5, v179, v161, v191
	v_pk_fma_f32 v[2:3], v[176:177], v[158:159], v[188:189]
	v_pk_fma_f32 v[32:33], v[30:31], v[26:27], v[202:203]
	v_pk_fma_f32 v[30:31], v[28:29], v[22:23], v[200:201]
	v_pk_fma_f32 v[28:29], v[186:187], v[20:21], v[198:199]
	v_pk_fma_f32 v[26:27], v[184:185], v[18:19], v[196:197]
	v_pk_fma_f32 v[24:25], v[182:183], v[24:25], v[194:195]
	v_pk_fma_f32 v[22:23], v[180:181], v[166:167], v[192:193]
	v_pk_fma_f32 v[20:21], v[178:179], v[164:165], v[190:191]
	v_pk_fma_f32 v[18:19], v[176:177], v[162:163], v[188:189]
	ds_read_b128 v[158:161], v174 offset:33696
	ds_read_b128 v[162:165], v174 offset:33728
	ds_read_b128 v[166:169], v174 offset:33952
	ds_read_b128 v[176:179], v174 offset:33984
	ds_read_b128 v[180:183], v174 offset:34016
	ds_read_b128 v[184:187], v212 offset:11264
	v_mfma_f32_32x32x16_bf16 v[34:49], v[208:211], v[138:141], v[34:49]
	v_cvt_pk_bf16_f32 v86, v86, v87
	v_cvt_pk_bf16_f32 v87, v88, v89
	v_cvt_pk_bf16_f32 v88, v90, v91
	v_cvt_pk_bf16_f32 v89, v92, v93
	ds_read_b128 v[90:93], v212 offset:12288
	v_pk_max_i16 v86, v86, 0
	v_pk_max_i16 v87, v87, 0
	v_pk_max_i16 v88, v88, 0
	v_pk_max_i16 v89, v89, 0
	s_nop 1
	s_nop 0
	v_cvt_pk_bf16_f32 v188, v34, v35
	v_cvt_pk_bf16_f32 v189, v36, v37
	v_cvt_pk_bf16_f32 v190, v38, v39
	v_cvt_pk_bf16_f32 v191, v40, v41
	s_waitcnt lgkmcnt(1)
	v_mfma_f32_32x32x16_bf16 v[2:17], v[184:187], v[86:89], v[2:17]
	v_pk_max_i16 v188, v188, 0
	v_pk_max_i16 v189, v189, 0
	v_pk_max_i16 v190, v190, 0
	v_pk_max_i16 v191, v191, 0
	v_cvt_pk_bf16_f32 v94, v94, v95
	v_cvt_pk_bf16_f32 v95, v96, v97
	v_cvt_pk_bf16_f32 v96, v98, v99
	v_cvt_pk_bf16_f32 v97, v100, v101
	v_cvt_pk_bf16_f32 v98, v42, v43
	v_cvt_pk_bf16_f32 v99, v44, v45
	v_mfma_f32_32x32x16_bf16 v[18:33], v[184:187], v[188:191], v[18:33]
	ds_read_b128 v[184:187], v212 offset:19456
	v_cvt_pk_bf16_f32 v100, v46, v47
	v_cvt_pk_bf16_f32 v101, v48, v49
	v_fma_f32 v64, v80, v64, v182
	v_fma_f32 v65, v81, v65, v183
	v_pk_fma_f32 v[62:63], v[78:79], v[62:63], v[180:181]
	v_pk_fma_f32 v[60:61], v[164:165], v[60:61], v[178:179]
	v_pk_fma_f32 v[58:59], v[162:163], v[58:59], v[176:177]
	v_pk_max_i16 v94, v94, 0
	v_pk_max_i16 v95, v95, 0
	v_pk_max_i16 v96, v96, 0
	v_pk_max_i16 v97, v97, 0
	v_pk_max_i16 v98, v98, 0
	v_pk_max_i16 v99, v99, 0
	v_pk_max_i16 v100, v100, 0
	v_pk_max_i16 v101, v101, 0
	v_pk_fma_f32 v[56:57], v[160:161], v[56:57], v[168:169]
	s_waitcnt lgkmcnt(1)
	v_mfma_f32_32x32x16_bf16 v[2:17], v[90:93], v[94:97], v[2:17]
	v_fma_f32 v54, v158, v54, v166
	v_fma_f32 v55, v159, v55, v167
	v_fma_f32 v52, v72, v52, v76
	v_fma_f32 v53, v73, v53, v77
	v_fma_f32 v50, v70, v50, v74
	v_fma_f32 v51, v71, v51, v75
	v_pk_fma_f32 v[48:49], v[80:81], v[156:157], v[182:183]
	v_pk_fma_f32 v[46:47], v[78:79], v[114:115], v[180:181]
	v_pk_fma_f32 v[44:45], v[164:165], v[110:111], v[178:179]
	v_pk_fma_f32 v[42:43], v[162:163], v[102:103], v[176:177]
	v_mfma_f32_32x32x16_bf16 v[18:33], v[90:93], v[98:101], v[18:33]
	ds_read_b128 v[90:93], v212 offset:20480
	v_fma_f32 v40, v160, v154, v168
	v_fma_f32 v41, v161, v155, v169
	v_fma_f32 v38, v158, v116, v166
	v_fma_f32 v39, v159, v117, v167
	v_pk_fma_f32 v[36:37], v[72:73], v[112:113], v[76:77]
	v_pk_fma_f32 v[34:35], v[70:71], v[104:105], v[74:75]
	s_waitcnt lgkmcnt(1)
	v_mfma_f32_32x32x16_bf16 v[50:65], v[184:187], v[86:89], v[50:65]
	ds_read_b128 v[70:73], v174 offset:32928
	ds_read_b128 v[74:77], v174 offset:32960
	ds_read_b128 v[78:81], v174 offset:32992
	ds_read_b128 v[86:89], v174 offset:33024
	ds_read_b128 v[110:113], v212 offset:1024
	v_mfma_f32_32x32x16_bf16 v[34:49], v[184:187], v[188:191], v[34:49]
	s_waitcnt lgkmcnt(5)
	v_mfma_f32_32x32x16_bf16 v[50:65], v[90:93], v[94:97], v[50:65]
	v_mfma_f32_32x32x16_bf16 v[34:49], v[90:93], v[98:101], v[34:49]
	s_waitcnt lgkmcnt(2)
	v_mfma_f32_32x32x16_bf16 v[90:105], v[106:109], v[126:129], v[66:81]
	v_mfma_f32_32x32x16_bf16 v[66:81], v[106:109], v[134:137], v[66:81]
	ds_read_b128 v[106:109], v212 offset:0
	s_waitcnt lgkmcnt(0)
	v_mfma_f32_32x32x16_bf16 v[90:105], v[106:109], v[122:125], v[90:105]
	v_mfma_f32_32x32x16_bf16 v[66:81], v[106:109], v[146:149], v[66:81]
	ds_read_b128 v[106:109], v212 offset:2048
	v_mfma_f32_32x32x16_bf16 v[90:105], v[110:113], v[130:133], v[90:105]
	v_mfma_f32_32x32x16_bf16 v[66:81], v[110:113], v[142:145], v[66:81]
	ds_read_b128 v[110:113], v212 offset:13312
	s_waitcnt lgkmcnt(1)
	v_mfma_f32_32x32x16_bf16 v[90:105], v[106:109], v[118:121], v[90:105]
	v_mfma_f32_32x32x16_bf16 v[66:81], v[106:109], v[138:141], v[66:81]
	s_nop 10
	v_cvt_pk_bf16_f32 v90, v90, v91
	v_cvt_pk_bf16_f32 v91, v92, v93
	v_cvt_pk_bf16_f32 v92, v94, v95
	v_cvt_pk_bf16_f32 v94, v98, v99
	v_cvt_pk_bf16_f32 v95, v100, v101
	ds_read_b128 v[98:101], v212 offset:21504
	v_cvt_pk_bf16_f32 v66, v66, v67
	v_cvt_pk_bf16_f32 v67, v68, v69
	v_cvt_pk_bf16_f32 v68, v70, v71
	v_cvt_pk_bf16_f32 v93, v96, v97
	v_cvt_pk_bf16_f32 v69, v72, v73
	ds_read_b128 v[70:73], v212 offset:14336
	v_pk_max_i16 v90, v90, 0
	v_pk_max_i16 v91, v91, 0
	v_pk_max_i16 v92, v92, 0
	v_pk_max_i16 v93, v93, 0
	v_pk_max_i16 v66, v66, 0
	v_pk_max_i16 v67, v67, 0
	v_pk_max_i16 v68, v68, 0
	v_pk_max_i16 v69, v69, 0
	v_cvt_pk_bf16_f32 v96, v102, v103
	s_waitcnt lgkmcnt(2)
	v_mfma_f32_32x32x16_bf16 v[2:17], v[110:113], v[90:93], v[2:17]
	v_cvt_pk_bf16_f32 v97, v104, v105
	v_cvt_pk_bf16_f32 v74, v74, v75
	v_cvt_pk_bf16_f32 v75, v76, v77
	v_cvt_pk_bf16_f32 v76, v78, v79
	v_cvt_pk_bf16_f32 v77, v80, v81
	v_pk_max_i16 v94, v94, 0
	v_pk_max_i16 v95, v95, 0
	v_pk_max_i16 v96, v96, 0
	v_pk_max_i16 v97, v97, 0
	v_pk_max_i16 v74, v74, 0
	v_pk_max_i16 v75, v75, 0
	v_pk_max_i16 v76, v76, 0
	v_pk_max_i16 v77, v77, 0
	v_mfma_f32_32x32x16_bf16 v[18:33], v[110:113], v[66:69], v[18:33]
	s_waitcnt lgkmcnt(1)
	v_mfma_f32_32x32x16_bf16 v[34:49], v[98:101], v[66:69], v[34:49]
	ds_read_b128 v[66:69], v212 offset:22528
	v_mfma_f32_32x32x16_bf16 v[50:65], v[98:101], v[90:93], v[50:65]
	s_waitcnt lgkmcnt(1)
	v_mfma_f32_32x32x16_bf16 v[2:17], v[70:73], v[94:97], v[2:17]
	v_mfma_f32_32x32x16_bf16 v[18:33], v[70:73], v[74:77], v[18:33]
	ds_read_b128 v[78:81], v212 offset:3072
	s_waitcnt lgkmcnt(1)
	v_mfma_f32_32x32x16_bf16 v[50:65], v[66:69], v[94:97], v[50:65]
	ds_read_b128 v[90:93], v174 offset:33056
	ds_read_b128 v[94:97], v174 offset:33088
	ds_read_b128 v[98:101], v174 offset:33120
	ds_read_b128 v[70:73], v174 offset:33152
	v_mfma_f32_32x32x16_bf16 v[34:49], v[66:69], v[74:77], v[34:49]
	ds_read_b128 v[66:69], v212 offset:4096
	ds_read_b128 v[74:77], v212 offset:5120
	s_waitcnt lgkmcnt(3)
	v_mfma_f32_32x32x16_bf16 v[102:117], v[78:81], v[126:129], v[86:101]
	v_mfma_f32_32x32x16_bf16 v[86:101], v[78:81], v[134:137], v[86:101]
	s_waitcnt lgkmcnt(1)
	v_mfma_f32_32x32x16_bf16 v[86:101], v[66:69], v[146:149], v[86:101]
	v_mfma_f32_32x32x16_bf16 v[102:117], v[66:69], v[122:125], v[102:117]
	ds_read_b128 v[66:69], v212 offset:6144
	s_waitcnt lgkmcnt(1)
	v_mfma_f32_32x32x16_bf16 v[86:101], v[74:77], v[142:145], v[86:101]
	v_mfma_f32_32x32x16_bf16 v[102:117], v[74:77], v[130:133], v[102:117]
	ds_read_b128 v[74:77], v212 offset:15360
	s_waitcnt lgkmcnt(1)
	v_mfma_f32_32x32x16_bf16 v[86:101], v[66:69], v[138:141], v[86:101]
	v_mfma_f32_32x32x16_bf16 v[102:117], v[66:69], v[118:121], v[102:117]
	s_nop 10
	v_cvt_pk_bf16_f32 v78, v86, v87
	v_cvt_pk_bf16_f32 v80, v90, v91
	v_cvt_pk_bf16_f32 v79, v88, v89
	v_cvt_pk_bf16_f32 v81, v92, v93
	ds_read_b128 v[86:89], v212 offset:16384
	ds_read_b128 v[90:93], v212 offset:23552
	v_cvt_pk_bf16_f32 v66, v102, v103
	v_cvt_pk_bf16_f32 v67, v104, v105
	v_cvt_pk_bf16_f32 v68, v106, v107
	v_cvt_pk_bf16_f32 v69, v108, v109
	v_pk_max_i16 v66, v66, 0
	v_pk_max_i16 v67, v67, 0
	v_pk_max_i16 v68, v68, 0
	v_pk_max_i16 v69, v69, 0
	v_pk_max_i16 v78, v78, 0
	v_pk_max_i16 v79, v79, 0
	v_pk_max_i16 v80, v80, 0
	v_pk_max_i16 v81, v81, 0
	v_cvt_pk_bf16_f32 v94, v94, v95
	s_waitcnt lgkmcnt(2)
	v_mfma_f32_32x32x16_bf16 v[18:33], v[74:77], v[78:81], v[18:33]
	v_cvt_pk_bf16_f32 v95, v96, v97
	v_cvt_pk_bf16_f32 v96, v98, v99
	v_cvt_pk_bf16_f32 v97, v100, v101
	v_pk_max_i16 v94, v94, 0
	v_pk_max_i16 v95, v95, 0
	v_pk_max_i16 v96, v96, 0
	v_pk_max_i16 v97, v97, 0
	v_mfma_f32_32x32x16_bf16 v[2:17], v[74:77], v[66:69], v[2:17]
	v_cvt_pk_bf16_f32 v74, v110, v111
	v_cvt_pk_bf16_f32 v75, v112, v113
	v_cvt_pk_bf16_f32 v76, v114, v115
	v_cvt_pk_bf16_f32 v77, v116, v117
	v_pk_max_i16 v74, v74, 0
	v_pk_max_i16 v75, v75, 0
	v_pk_max_i16 v76, v76, 0
	v_pk_max_i16 v77, v77, 0
	s_waitcnt lgkmcnt(0)
	v_mfma_f32_32x32x16_bf16 v[50:65], v[90:93], v[66:69], v[50:65]
	ds_read_b128 v[66:69], v212 offset:24576
	v_mfma_f32_32x32x16_bf16 v[34:49], v[90:93], v[78:81], v[34:49]
	ds_read_b128 v[102:105], v212 offset:7168
	v_mfma_f32_32x32x16_bf16 v[2:17], v[86:89], v[74:77], v[2:17]
	s_waitcnt lgkmcnt(1)
	v_mfma_f32_32x32x16_bf16 v[50:65], v[66:69], v[74:77], v[50:65]
	ds_read_b128 v[74:77], v174 offset:33184
	ds_read_b128 v[78:81], v174 offset:33216
	v_mfma_f32_32x32x16_bf16 v[34:49], v[66:69], v[94:97], v[34:49]
	ds_read_b128 v[66:69], v212 offset:8192
	v_mfma_f32_32x32x16_bf16 v[18:33], v[86:89], v[94:97], v[18:33]
	s_waitcnt lgkmcnt(1)
	v_mfma_f32_32x32x16_bf16 v[86:101], v[102:105], v[126:129], v[70:85]
	v_mfma_f32_32x32x16_bf16 v[70:85], v[102:105], v[134:137], v[70:85]
	ds_read_b128 v[102:105], v212 offset:9216
	v_lshlrev_b32_e32 v135, 2, v1
	v_add_u32_e32 v134, v172, v174
	s_waitcnt lgkmcnt(1)
	v_mfma_f32_32x32x16_bf16 v[86:101], v[66:69], v[122:125], v[86:101]
	v_mfma_f32_32x32x16_bf16 v[70:85], v[66:69], v[146:149], v[70:85]
	ds_read_b128 v[66:69], v212 offset:10240
	s_waitcnt lgkmcnt(1)
	v_mfma_f32_32x32x16_bf16 v[86:101], v[102:105], v[130:133], v[86:101]
	v_mfma_f32_32x32x16_bf16 v[70:85], v[102:105], v[142:145], v[70:85]
	ds_read_b128 v[102:105], v212 offset:17408
	s_waitcnt lgkmcnt(1)
	v_mfma_f32_32x32x16_bf16 v[86:101], v[66:69], v[118:121], v[86:101]
	v_mfma_f32_32x32x16_bf16 v[70:85], v[66:69], v[138:141], v[70:85]
	s_nop 10
	v_cvt_pk_bf16_f32 v68, v90, v91
	v_cvt_pk_bf16_f32 v69, v92, v93
	ds_read_b128 v[90:93], v212 offset:25600
	v_cvt_pk_bf16_f32 v66, v86, v87
	v_cvt_pk_bf16_f32 v67, v88, v89
	v_pk_max_i16 v66, v66, 0
	v_pk_max_i16 v67, v67, 0
	v_pk_max_i16 v68, v68, 0
	v_pk_max_i16 v69, v69, 0
	v_cvt_pk_bf16_f32 v70, v70, v71
	v_cvt_pk_bf16_f32 v71, v72, v73
	s_waitcnt lgkmcnt(1)
	v_mfma_f32_32x32x16_bf16 v[2:17], v[102:105], v[66:69], v[2:17]
	v_cvt_pk_bf16_f32 v72, v74, v75
	v_cvt_pk_bf16_f32 v73, v76, v77
	ds_read_b128 v[74:77], v212 offset:18432
	v_cvt_pk_bf16_f32 v86, v94, v95
	v_cvt_pk_bf16_f32 v87, v96, v97
	v_cvt_pk_bf16_f32 v88, v98, v99
	s_waitcnt lgkmcnt(1)
	v_mfma_f32_32x32x16_bf16 v[50:65], v[90:93], v[66:69], v[50:65]
	ds_read_b128 v[66:69], v212 offset:26624
	v_cvt_pk_bf16_f32 v89, v100, v101
	v_pk_max_i16 v86, v86, 0
	v_pk_max_i16 v87, v87, 0
	v_pk_max_i16 v88, v88, 0
	v_pk_max_i16 v89, v89, 0
	v_pk_max_i16 v70, v70, 0
	v_pk_max_i16 v71, v71, 0
	v_pk_max_i16 v72, v72, 0
	v_pk_max_i16 v73, v73, 0
	v_cvt_pk_bf16_f32 v78, v78, v79
	v_cvt_pk_bf16_f32 v79, v80, v81
	s_waitcnt lgkmcnt(1)
	v_mfma_f32_32x32x16_bf16 v[2:17], v[74:77], v[86:89], v[2:17]
	v_cvt_pk_bf16_f32 v80, v82, v83
	v_cvt_pk_bf16_f32 v81, v84, v85
	v_pk_max_i16 v78, v78, 0
	v_pk_max_i16 v79, v79, 0
	v_pk_max_i16 v80, v80, 0
	v_pk_max_i16 v81, v81, 0
	s_waitcnt lgkmcnt(0)
	v_mfma_f32_32x32x16_bf16 v[50:65], v[66:69], v[86:89], v[50:65]
	v_mfma_f32_32x32x16_bf16 v[34:49], v[90:93], v[70:73], v[34:49]
	s_nop 10
	v_add_f32_e32 v130, v10, v58
	v_add_f32_e32 v131, v11, v59
	v_add_f32_e32 v132, v12, v60
	v_add_f32_e32 v133, v13, v61
	v_add_f32_e32 v138, v4, v52
	v_add_f32_e32 v139, v5, v53
	v_pk_add_f32 v[140:141], v[16:17], v[64:65]
	v_pk_add_f32 v[142:143], v[8:9], v[56:57]
	v_pk_add_f32 v[144:145], v[14:15], v[62:63]
	v_pk_add_f32 v[146:147], v[6:7], v[54:55]
	v_mfma_f32_32x32x16_bf16 v[18:33], v[102:105], v[70:73], v[18:33]
	ds_read2st64_b32 v[70:71], v135 offset0:133 offset1:134
	v_add_f32_e32 v148, v2, v50
	v_add_f32_e32 v149, v3, v51
	v_add_f32_e32 v144, v146, v144
	v_add_f32_e32 v145, v147, v145
	v_pk_add_f32 v[140:141], v[142:143], v[140:141]
	v_pk_add_f32 v[132:133], v[138:139], v[132:133]
	v_pk_add_f32 v[130:131], v[148:149], v[130:131]
	v_pk_add_f32 v[132:133], v[132:133], v[140:141]
	v_pk_add_f32 v[130:131], v[130:131], v[144:145]
	v_mfma_f32_32x32x16_bf16 v[34:49], v[66:69], v[78:81], v[34:49]
	v_pk_mov_b32 v[138:139], v[130:131], v[132:133] op_sel:[1,0]
	v_mov_b32_e32 v131, v133
	s_waitcnt vmcnt(0) lgkmcnt(0)
	v_mul_f32_e32 v66, v175, v70
	v_pk_add_f32 v[130:131], v[138:139], v[130:131]
	ds_write_b32 v173, v66 offset:512
	v_mul_f32_e32 v66, v175, v71
	v_pk_add_f32 v[130:131], v[130:131], v[130:131] op_sel:[0,1] op_sel_hi:[1,0]
	s_waitcnt lgkmcnt(0)
	ds_read_b128 v[102:105], v174 offset:34560
	ds_read_b128 v[98:101], v174 offset:34592
	ds_read_b128 v[110:113], v174 offset:34624
	ds_read_b128 v[106:109], v174 offset:34656
	ds_read_b128 v[114:117], v174 offset:34688
	ds_read_b128 v[122:125], v174 offset:34720
	ds_read_b128 v[118:121], v174 offset:34752
	ds_read_b128 v[126:129], v174 offset:34784
	v_mov_b32_dpp v66, v66 quad_perm:[1,0,3,2] row_mask:0xf bank_mask:0xf bound_ctrl:1
	v_mov_b32_e32 v131, v130
	v_fmac_f32_e32 v66, v175, v71
	s_nop 0
	v_permlane32_swap_b32_e32 v130, v131
	v_add_f32_dpp v66, v66, v66 quad_perm:[2,3,0,1] row_mask:0xf bank_mask:0xf bound_ctrl:1
	v_add_f32_e32 v130, v130, v131
	v_fmamk_f32 v65, v130, 0xbc800000, v65
	v_add_f32_dpp v66, v66, v66 row_half_mirror row_mask:0xf bank_mask:0xf bound_ctrl:1
	v_fmamk_f32 v64, v130, 0xbc800000, v64
	v_fmamk_f32 v63, v130, 0xbc800000, v63
	v_fmamk_f32 v62, v130, 0xbc800000, v62
	v_fmamk_f32 v61, v130, 0xbc800000, v61
	v_fmamk_f32 v60, v130, 0xbc800000, v60
	v_fmamk_f32 v59, v130, 0xbc800000, v59
	v_fmamk_f32 v58, v130, 0xbc800000, v58
	v_fmamk_f32 v57, v130, 0xbc800000, v57
	v_fmamk_f32 v56, v130, 0xbc800000, v56
	v_fmamk_f32 v55, v130, 0xbc800000, v55
	v_fmamk_f32 v54, v130, 0xbc800000, v54
	v_fmamk_f32 v53, v130, 0xbc800000, v53
	v_fmamk_f32 v52, v130, 0xbc800000, v52
	v_fmamk_f32 v51, v130, 0xbc800000, v51
	v_fmac_f32_e32 v50, 0xbc800000, v130
	v_add_f32_dpp v66, v66, v66 row_ror:8 row_mask:0xf bank_mask:0xf bound_ctrl:1
	v_fmamk_f32 v17, v130, 0xbc800000, v17
	v_fmamk_f32 v16, v130, 0xbc800000, v16
	v_fmamk_f32 v15, v130, 0xbc800000, v15
	v_fmamk_f32 v14, v130, 0xbc800000, v14
	v_fmamk_f32 v13, v130, 0xbc800000, v13
	v_fmamk_f32 v12, v130, 0xbc800000, v12
	v_fmamk_f32 v11, v130, 0xbc800000, v11
	v_fmamk_f32 v10, v130, 0xbc800000, v10
	v_fmamk_f32 v9, v130, 0xbc800000, v9
	v_fmamk_f32 v8, v130, 0xbc800000, v8
	v_fmamk_f32 v7, v130, 0xbc800000, v7
	v_fmamk_f32 v6, v130, 0xbc800000, v6
	v_fmamk_f32 v5, v130, 0xbc800000, v5
	v_fmamk_f32 v4, v130, 0xbc800000, v4
	v_fmamk_f32 v3, v130, 0xbc800000, v3
	v_fmac_f32_e32 v2, 0xbc800000, v130
	v_pk_mul_f32 v[130:131], v[54:55], v[54:55]
	v_pk_mul_f32 v[132:133], v[62:63], v[62:63]
	v_pk_mul_f32 v[138:139], v[50:51], v[50:51]
	v_pk_mul_f32 v[140:141], v[58:59], v[58:59]
	v_pk_mul_f32 v[142:143], v[56:57], v[56:57]
	v_pk_mul_f32 v[144:145], v[64:65], v[64:65]
	v_pk_mul_f32 v[146:147], v[52:53], v[52:53]
	v_pk_mul_f32 v[148:149], v[60:61], v[60:61]
	v_mov_b32_e32 v67, v66
	v_pk_fma_f32 v[148:149], v[12:13], v[12:13], v[148:149]
	v_pk_fma_f32 v[146:147], v[4:5], v[4:5], v[146:147]
	v_pk_fma_f32 v[144:145], v[16:17], v[16:17], v[144:145]
	v_pk_fma_f32 v[142:143], v[8:9], v[8:9], v[142:143]
	v_pk_fma_f32 v[140:141], v[10:11], v[10:11], v[140:141]
	v_pk_fma_f32 v[138:139], v[2:3], v[2:3], v[138:139]
	v_pk_fma_f32 v[132:133], v[14:15], v[14:15], v[132:133]
	v_pk_fma_f32 v[130:131], v[6:7], v[6:7], v[130:131]
	v_permlane16_swap_b32_e32 v66, v67
	v_pk_add_f32 v[130:131], v[130:131], v[132:133]
	v_pk_add_f32 v[132:133], v[138:139], v[140:141]
	v_pk_add_f32 v[138:139], v[142:143], v[144:145]
	v_pk_add_f32 v[140:141], v[146:147], v[148:149]
	v_mfma_f32_32x32x16_bf16 v[18:33], v[74:77], v[78:81], v[18:33]
	v_add_f32_e32 v136, v66, v67
	ds_read_b128 v[70:73], v134 offset:512
	ds_read_b128 v[66:69], v134 offset:544
	ds_read_b128 v[78:81], v134 offset:576
	ds_read_b128 v[74:77], v134 offset:608
	ds_read_b128 v[82:85], v134 offset:640
	ds_read_b128 v[90:93], v134 offset:672
	ds_read_b128 v[86:89], v134 offset:704
	ds_read_b128 v[94:97], v134 offset:736
	v_pk_add_f32 v[138:139], v[140:141], v[138:139]
	v_pk_add_f32 v[130:131], v[132:133], v[130:131]
	s_waitcnt lgkmcnt(8)
	v_pk_mul_f32 v[140:141], v[126:127], v[62:63]
	v_pk_mov_b32 v[132:133], v[130:131], v[138:139] op_sel:[1,0]
	v_mov_b32_e32 v131, v139
	v_pk_mul_f32 v[138:139], v[122:123], v[54:55]
	v_pk_mul_f32 v[142:143], v[114:115], v[50:51]
	v_pk_mul_f32 v[144:145], v[118:119], v[58:59]
	v_pk_mul_f32 v[146:147], v[124:125], v[56:57]
	v_pk_mul_f32 v[148:149], v[128:129], v[64:65]
	v_pk_mul_f32 v[154:155], v[116:117], v[52:53]
	v_pk_mul_f32 v[156:157], v[120:121], v[60:61]
	v_pk_fma_f32 v[154:155], v[104:105], v[4:5], v[154:155]
	v_pk_fma_f32 v[156:157], v[112:113], v[12:13], v[156:157]
	v_pk_fma_f32 v[148:149], v[108:109], v[16:17], v[148:149]
	v_pk_fma_f32 v[146:147], v[100:101], v[8:9], v[146:147]
	v_pk_fma_f32 v[144:145], v[110:111], v[10:11], v[144:145]
	v_pk_fma_f32 v[142:143], v[102:103], v[2:3], v[142:143]
	v_pk_fma_f32 v[140:141], v[106:107], v[14:15], v[140:141]
	v_pk_fma_f32 v[138:139], v[98:99], v[6:7], v[138:139]
	v_pk_add_f32 v[130:131], v[132:133], v[130:131]
	v_pk_add_f32 v[138:139], v[138:139], v[140:141]
	v_pk_add_f32 v[140:141], v[142:143], v[144:145]
	v_pk_add_f32 v[142:143], v[146:147], v[148:149]
	v_pk_add_f32 v[144:145], v[154:155], v[156:157]
	v_pk_add_f32 v[132:133], v[130:131], v[130:131] op_sel:[0,1] op_sel_hi:[1,0]
	v_pk_add_f32 v[142:143], v[144:145], v[142:143]
	v_pk_add_f32 v[138:139], v[140:141], v[138:139]
	v_add_f32_e32 v133, v142, v143
	v_add_f32_e32 v130, v138, v139
	s_waitcnt lgkmcnt(2)
	v_pk_mul_f32 v[138:139], v[90:91], v[54:55]
	s_waitcnt lgkmcnt(0)
	v_pk_mul_f32 v[140:141], v[94:95], v[62:63]
	v_pk_mul_f32 v[142:143], v[82:83], v[50:51]
	v_pk_mul_f32 v[144:145], v[86:87], v[58:59]
	v_pk_mul_f32 v[146:147], v[92:93], v[56:57]
	v_pk_mul_f32 v[148:149], v[96:97], v[64:65]
	v_pk_mul_f32 v[154:155], v[84:85], v[52:53]
	v_pk_mul_f32 v[156:157], v[88:89], v[60:61]
	v_add_f32_e32 v130, v130, v133
	v_pk_fma_f32 v[156:157], v[80:81], v[12:13], v[156:157]
	v_pk_fma_f32 v[154:155], v[72:73], v[4:5], v[154:155]
	v_pk_fma_f32 v[148:149], v[76:77], v[16:17], v[148:149]
	v_pk_fma_f32 v[146:147], v[68:69], v[8:9], v[146:147]
	v_pk_fma_f32 v[144:145], v[78:79], v[10:11], v[144:145]
	v_pk_fma_f32 v[142:143], v[70:71], v[2:3], v[142:143]
	v_pk_fma_f32 v[140:141], v[74:75], v[14:15], v[140:141]
	v_pk_fma_f32 v[138:139], v[66:67], v[6:7], v[138:139]
	v_mov_b32_e32 v133, v130
	v_pk_add_f32 v[138:139], v[138:139], v[140:141]
	v_pk_add_f32 v[140:141], v[142:143], v[144:145]
	v_pk_add_f32 v[142:143], v[146:147], v[148:149]
	v_pk_add_f32 v[144:145], v[154:155], v[156:157]
	v_permlane32_swap_b32_e32 v130, v133
	v_pk_add_f32 v[142:143], v[144:145], v[142:143]
	v_add_f32_e32 v160, v130, v133
	v_pk_add_f32 v[138:139], v[140:141], v[138:139]
	v_add_f32_e32 v133, v142, v143
	v_pk_add_f32 v[140:141], v[26:27], v[42:43]
	v_pk_add_f32 v[142:143], v[28:29], v[44:45]
	v_pk_add_f32 v[144:145], v[20:21], v[36:37]
	v_pk_add_f32 v[146:147], v[32:33], v[48:49]
	v_pk_add_f32 v[148:149], v[24:25], v[40:41]
	v_pk_add_f32 v[154:155], v[30:31], v[46:47]
	v_pk_add_f32 v[156:157], v[22:23], v[38:39]
	v_pk_add_f32 v[158:159], v[18:19], v[34:35]
	v_pk_add_f32 v[154:155], v[156:157], v[154:155]
	v_pk_add_f32 v[146:147], v[148:149], v[146:147]
	v_pk_add_f32 v[142:143], v[144:145], v[142:143]
	v_pk_add_f32 v[140:141], v[158:159], v[140:141]
	v_pk_add_f32 v[142:143], v[142:143], v[146:147]
	v_pk_add_f32 v[140:141], v[140:141], v[154:155]
	v_add_f32_e32 v130, v138, v139
	v_pk_mov_b32 v[144:145], v[140:141], v[142:143] op_sel:[1,0]
	v_mov_b32_e32 v141, v143
	v_pk_add_f32 v[140:141], v[144:145], v[140:141]
	v_add_f32_e32 v133, v130, v133
	v_pk_add_f32 v[140:141], v[140:141], v[140:141] op_sel:[0,1] op_sel_hi:[1,0]
	v_mov_b32_e32 v131, v132
	v_mov_b32_e32 v130, v140
	s_nop 1
	v_permlane32_swap_b32_e32 v140, v130
	v_add_f32_e32 v130, v140, v130
	v_fmamk_f32 v49, v130, 0xbc800000, v49
	v_fmamk_f32 v48, v130, 0xbc800000, v48
	v_fmamk_f32 v47, v130, 0xbc800000, v47
	v_fmamk_f32 v46, v130, 0xbc800000, v46
	v_fmamk_f32 v45, v130, 0xbc800000, v45
	v_fmamk_f32 v44, v130, 0xbc800000, v44
	v_fmamk_f32 v43, v130, 0xbc800000, v43
	v_fmamk_f32 v42, v130, 0xbc800000, v42
	v_fmamk_f32 v41, v130, 0xbc800000, v41
	v_fmamk_f32 v40, v130, 0xbc800000, v40
	v_fmamk_f32 v39, v130, 0xbc800000, v39
	v_fmamk_f32 v38, v130, 0xbc800000, v38
	v_fmamk_f32 v37, v130, 0xbc800000, v37
	v_fmamk_f32 v36, v130, 0xbc800000, v36
	v_fmamk_f32 v35, v130, 0xbc800000, v35
	v_fmac_f32_e32 v34, 0xbc800000, v130
	v_fmamk_f32 v33, v130, 0xbc800000, v33
	v_fmamk_f32 v32, v130, 0xbc800000, v32
	v_fmamk_f32 v31, v130, 0xbc800000, v31
	v_fmamk_f32 v30, v130, 0xbc800000, v30
	v_fmamk_f32 v29, v130, 0xbc800000, v29
	v_fmamk_f32 v28, v130, 0xbc800000, v28
	v_fmamk_f32 v27, v130, 0xbc800000, v27
	v_fmamk_f32 v26, v130, 0xbc800000, v26
	v_fmamk_f32 v25, v130, 0xbc800000, v25
	v_fmamk_f32 v24, v130, 0xbc800000, v24
	v_fmamk_f32 v23, v130, 0xbc800000, v23
	v_fmamk_f32 v22, v130, 0xbc800000, v22
	v_fmamk_f32 v21, v130, 0xbc800000, v21
	v_fmamk_f32 v20, v130, 0xbc800000, v20
	v_fmamk_f32 v19, v130, 0xbc800000, v19
	v_fmac_f32_e32 v18, 0xbc800000, v130
	v_pk_mul_f32 v[140:141], v[38:39], v[38:39]
	v_pk_mul_f32 v[142:143], v[46:47], v[46:47]
	v_pk_mul_f32 v[144:145], v[34:35], v[34:35]
	v_pk_mul_f32 v[146:147], v[42:43], v[42:43]
	v_pk_mul_f32 v[148:149], v[40:41], v[40:41]
	v_pk_mul_f32 v[154:155], v[48:49], v[48:49]
	v_pk_mul_f32 v[156:157], v[36:37], v[36:37]
	v_pk_mul_f32 v[158:159], v[44:45], v[44:45]
	v_pk_fma_f32 v[156:157], v[20:21], v[20:21], v[156:157]
	v_pk_fma_f32 v[158:159], v[28:29], v[28:29], v[158:159]
	v_pk_fma_f32 v[154:155], v[32:33], v[32:33], v[154:155]
	v_pk_fma_f32 v[148:149], v[24:25], v[24:25], v[148:149]
	v_pk_fma_f32 v[146:147], v[26:27], v[26:27], v[146:147]
	v_pk_fma_f32 v[144:145], v[18:19], v[18:19], v[144:145]
	v_pk_fma_f32 v[142:143], v[30:31], v[30:31], v[142:143]
	v_pk_fma_f32 v[140:141], v[22:23], v[22:23], v[140:141]
	v_permlane32_swap_b32_e32 v132, v131
	v_pk_add_f32 v[140:141], v[140:141], v[142:143]
	v_pk_add_f32 v[142:143], v[144:145], v[146:147]
	v_pk_add_f32 v[144:145], v[148:149], v[154:155]
	v_pk_add_f32 v[146:147], v[156:157], v[158:159]
	v_pk_add_f32 v[140:141], v[142:143], v[140:141]
	v_pk_add_f32 v[144:145], v[146:147], v[144:145]
	v_pk_mul_f32 v[122:123], v[122:123], v[38:39]
	v_pk_mov_b32 v[142:143], v[140:141], v[144:145] op_sel:[1,0]
	v_mov_b32_e32 v141, v145
	v_pk_add_f32 v[140:141], v[142:143], v[140:141]
	v_pk_mul_f32 v[126:127], v[126:127], v[46:47]
	v_pk_add_f32 v[140:141], v[140:141], v[140:141] op_sel:[0,1] op_sel_hi:[1,0]
	v_pk_mul_f32 v[114:115], v[114:115], v[34:35]
	v_mov_b32_e32 v130, v140
	s_nop 1
	v_permlane32_swap_b32_e32 v140, v130
	v_mov_b32_e32 v141, v132
	v_pk_add_f32 v[130:131], v[140:141], v[130:131]
	v_pk_mul_f32 v[118:119], v[118:119], v[42:43]
	v_pk_fma_f32 v[130:131], v[130:131], s[0:1], v[152:153] op_sel_hi:[1,0,0]
	v_pk_mul_f32 v[124:125], v[124:125], v[40:41]
	v_mul_f32_e32 v132, 0x4b800000, v131
	v_cmp_gt_f32_e32 vcc, s1, v131
	v_pk_mul_f32 v[128:129], v[128:129], v[48:49]
	v_pk_mul_f32 v[116:117], v[116:117], v[36:37]
	v_pk_mul_f32 v[120:121], v[120:121], v[44:45]
	v_cndmask_b32_e32 v131, v131, v132, vcc
	v_mul_f32_e32 v132, 0x4b800000, v130
	v_cmp_gt_f32_e64 s[0:1], s1, v130
	v_pk_fma_f32 v[112:113], v[112:113], v[28:29], v[120:121]
	v_pk_fma_f32 v[104:105], v[104:105], v[20:21], v[116:117]
	v_pk_fma_f32 v[108:109], v[108:109], v[32:33], v[128:129]
	v_pk_fma_f32 v[100:101], v[100:101], v[24:25], v[124:125]
	v_pk_fma_f32 v[110:111], v[110:111], v[26:27], v[118:119]
	v_pk_fma_f32 v[102:103], v[102:103], v[18:19], v[114:115]
	v_pk_fma_f32 v[106:107], v[106:107], v[30:31], v[126:127]
	v_pk_fma_f32 v[98:99], v[98:99], v[22:23], v[122:123]
	v_rsq_f32_e32 v131, v131
	v_cndmask_b32_e64 v130, v130, v132, s[0:1]
	v_pk_add_f32 v[98:99], v[98:99], v[106:107]
	v_pk_add_f32 v[102:103], v[102:103], v[110:111]
	v_pk_add_f32 v[100:101], v[100:101], v[108:109]
	v_pk_add_f32 v[104:105], v[104:105], v[112:113]
	v_rsq_f32_e32 v132, v130
	v_pk_add_f32 v[100:101], v[104:105], v[100:101]
	v_pk_add_f32 v[98:99], v[102:103], v[98:99]
	v_mul_f32_e32 v130, 0x45800000, v131
	v_add_f32_e32 v98, v98, v99
	v_add_f32_e32 v99, v100, v101
	v_add_f32_e32 v98, v98, v99
	v_mov_b32_e32 v99, v98
	v_pk_mul_f32 v[90:91], v[90:91], v[38:39]
	v_pk_mul_f32 v[94:95], v[94:95], v[46:47]
	v_pk_mul_f32 v[82:83], v[82:83], v[34:35]
	v_pk_mul_f32 v[86:87], v[86:87], v[42:43]
	v_cndmask_b32_e32 v130, v131, v130, vcc
	v_mul_f32_e32 v131, 0x45800000, v132
	v_permlane32_swap_b32_e32 v98, v99
	v_pk_fma_f32 v[78:79], v[78:79], v[26:27], v[86:87]
	v_pk_fma_f32 v[70:71], v[70:71], v[18:19], v[82:83]
	v_pk_fma_f32 v[74:75], v[74:75], v[30:31], v[94:95]
	v_pk_fma_f32 v[66:67], v[66:67], v[22:23], v[90:91]
	v_cndmask_b32_e64 v131, v132, v131, s[0:1]
	v_add_f32_e32 v98, v98, v99
	v_pk_add_f32 v[66:67], v[66:67], v[74:75]
	v_pk_add_f32 v[70:71], v[70:71], v[78:79]
	v_mul_f32_e32 v139, v160, v130
	v_mul_f32_e32 v98, v98, v131
	v_pk_add_f32 v[66:67], v[70:71], v[66:67]
	v_cmp_gt_u32_e32 vcc, 32, v1
	v_add_f32_e32 v66, v66, v67
	v_pk_mul_f32 v[92:93], v[92:93], v[40:41]
	v_cndmask_b32_e32 v67, v98, v139, vcc
	v_add_f32_e32 v67, s12, v67
	v_pk_mul_f32 v[96:97], v[96:97], v[48:49]
	v_pk_mul_f32 v[84:85], v[84:85], v[36:37]
	v_pk_mul_f32 v[88:89], v[88:89], v[44:45]
	v_mul_f32_e32 v67, 0xbfb8aa3b, v67
	v_pk_fma_f32 v[80:81], v[80:81], v[28:29], v[88:89]
	v_pk_fma_f32 v[72:73], v[72:73], v[20:21], v[84:85]
	v_pk_fma_f32 v[76:77], v[76:77], v[32:33], v[96:97]
	v_pk_fma_f32 v[68:69], v[68:69], v[24:25], v[92:93]
	v_exp_f32_e32 v70, v67
	v_pk_add_f32 v[68:69], v[68:69], v[76:77]
	v_pk_add_f32 v[72:73], v[72:73], v[80:81]
	v_cmp_lt_i32_e64 s[0:1], 0, v151
	v_pk_add_f32 v[68:69], v[72:73], v[68:69]
	v_mov_b32_e32 v137, v136
	v_add_f32_e32 v67, v68, v69
	v_add_f32_e32 v67, v66, v67
	v_add_f32_e32 v66, 1.0, v70
	v_rcp_f32_e32 v66, v66
	v_mov_b32_e32 v69, 0xff800000
	v_mov_b32_e32 v138, v133
	v_mov_b32_e32 v68, v67
	v_cndmask_b32_e64 v70, v69, v66, s[0:1]
	v_mbcnt_lo_u32_b32 v66, -1, 0
	v_mbcnt_hi_u32_b32 v66, -1, v66
	v_permlane32_swap_b32_e32 v136, v137
	v_permlane32_swap_b32_e32 v133, v138
	v_permlane32_swap_b32_e32 v67, v68
	v_and_b32_e32 v86, 64, v66
	s_mov_b32 s14, 8
	s_mov_b32 s13, 0
	v_mov_b32_e32 v66, 0
	s_waitcnt lgkmcnt(0)
